# expert-weight conversion loops: wait only for the current item's loads (next item's 32 loads stay in flight during the transpose)
# speedup vs baseline: 1.0693x; 1.0033x over previous
.LBB0_170:
	s_andn2_b64 vcc, exec, s[0:1]
	s_waitcnt vmcnt(4)
	v_mov_b32_e32 v14, v23
	v_mov_b32_e32 v15, v24
	v_mov_b32_e32 v16, v25
	v_mov_b32_e32 v17, v26
	v_mov_b32_e32 v18, v27
	v_mov_b32_e32 v20, v28
	v_mov_b32_e32 v19, v29
	v_mov_b32_e32 v21, v30
	v_mov_b32_e32 v22, v31
	v_mov_b32_e32 v32, v36
	v_mov_b32_e32 v33, v37
	v_mov_b32_e32 v38, v39
	v_mov_b32_e32 v40, v41
	v_mov_b32_e32 v43, v42
	v_mov_b32_e32 v44, v45
	v_mov_b32_e32 v47, v46
	v_mov_b32_e32 v49, v48
	v_mov_b32_e32 v52, v50
	v_mov_b32_e32 v53, v51
	v_mov_b32_e32 v56, v54
	v_mov_b32_e32 v58, v55
	v_mov_b32_e32 v61, v57
	v_mov_b32_e32 v62, v59
	v_mov_b32_e32 v65, v60
	v_mov_b32_e32 v67, v63
	v_mov_b32_e32 v70, v64
	v_mov_b32_e32 v71, v66
	v_mov_b32_e32 v74, v68
	v_mov_b32_e32 v76, v69
	v_mov_b32_e32 v77, v72
	v_mov_b32_e32 v78, v73
	v_mov_b32_e32 v79, v75
	s_cbranch_vccz .LBB0_183

.LBB0_181:
	s_waitcnt vmcnt(32)
	s_branch .Lmy_cvi_go

.Lmy_cvi_go:
	v_mul_f32_e32 v14, 0x42800000, v14
	v_mul_f32_e32 v15, 0x42800000, v15
	ds_write2_b32 v13, v14, v15 offset1:66
	v_mul_f32_e32 v14, 0x42800000, v16
	v_mul_f32_e32 v15, 0x42800000, v17
	ds_write2_b32 v13, v14, v15 offset0:132 offset1:198
	v_mul_f32_e32 v14, 0x42800000, v18
	v_mul_f32_e32 v15, 0x42800000, v20
	v_add_u32_e32 v16, 0x400, v13
	ds_write2_b32 v16, v14, v15 offset0:8 offset1:74
	v_mul_f32_e32 v14, 0x42800000, v19
	v_mul_f32_e32 v15, 0x42800000, v21
	ds_write2_b32 v16, v14, v15 offset0:140 offset1:206
	v_mul_f32_e32 v14, 0x42800000, v22
	v_mul_f32_e32 v15, 0x42800000, v32
	v_add_u32_e32 v16, 0x800, v13
	ds_write2_b32 v16, v14, v15 offset0:16 offset1:82
	v_mul_f32_e32 v14, 0x42800000, v33
	v_mul_f32_e32 v15, 0x42800000, v38
	ds_write2_b32 v16, v14, v15 offset0:148 offset1:214
	v_mul_f32_e32 v14, 0x42800000, v40
	v_mul_f32_e32 v15, 0x42800000, v43
	v_add_u32_e32 v16, 0xc00, v13
	ds_write2_b32 v16, v14, v15 offset0:24 offset1:90
	v_mul_f32_e32 v14, 0x42800000, v44
	v_mul_f32_e32 v15, 0x42800000, v47
	ds_write2_b32 v16, v14, v15 offset0:156 offset1:222
	v_mul_f32_e32 v14, 0x42800000, v49
	v_mul_f32_e32 v15, 0x42800000, v52
	v_add_u32_e32 v16, 0x1000, v13
	ds_write2_b32 v16, v14, v15 offset0:32 offset1:98
	v_mul_f32_e32 v14, 0x42800000, v53
	v_mul_f32_e32 v15, 0x42800000, v56
	ds_write2_b32 v16, v14, v15 offset0:164 offset1:230
	v_mul_f32_e32 v14, 0x42800000, v58
	v_mul_f32_e32 v15, 0x42800000, v61
	v_add_u32_e32 v16, 0x1400, v13
	ds_write2_b32 v16, v14, v15 offset0:40 offset1:106
	v_mul_f32_e32 v14, 0x42800000, v62
	v_mul_f32_e32 v15, 0x42800000, v65
	ds_write2_b32 v16, v14, v15 offset0:172 offset1:238
	v_mul_f32_e32 v14, 0x42800000, v67
	v_mul_f32_e32 v15, 0x42800000, v70
	v_add_u32_e32 v16, 0x1800, v13
	ds_write2_b32 v16, v14, v15 offset0:48 offset1:114
	v_mul_f32_e32 v14, 0x42800000, v71
	v_mul_f32_e32 v15, 0x42800000, v74
	ds_write2_b32 v16, v14, v15 offset0:180 offset1:246
	v_mul_f32_e32 v14, 0x42800000, v76
	v_mul_f32_e32 v15, 0x42800000, v77
	v_add_u32_e32 v16, 0x1c00, v13
	ds_write2_b32 v16, v14, v15 offset0:56 offset1:122
	v_mul_f32_e32 v14, 0x42800000, v78
	v_mul_f32_e32 v15, 0x42800000, v79
	ds_write2_b32 v16, v14, v15 offset0:188 offset1:254
	s_waitcnt lgkmcnt(0)
	ds_read2_b32 v[14:15], v1 offset1:8
	ds_read2_b32 v[16:17], v1 offset0:33 offset1:41
	ds_read2_b32 v[18:19], v1 offset0:66 offset1:74
	ds_read2_b32 v[20:21], v1 offset0:99 offset1:107
	ds_read2_b32 v[52:53], v1 offset0:132 offset1:140
	ds_read2_b32 v[70:71], v1 offset0:165 offset1:173
	s_waitcnt lgkmcnt(0)
	v_med3_f32 v14, v14, s13, v200
	v_med3_f32 v16, v16, s13, v200
	v_mov_b32_e32 v32, v35
	ds_read2_b32 v[76:77], v1 offset0:198 offset1:206
	ds_read2_b32 v[78:79], v1 offset0:231 offset1:239
	v_cvt_pk_fp8_f32 v32, v14, v16
	v_med3_f32 v14, v52, s13, v200
	v_med3_f32 v16, v70, s13, v200
	v_mov_b32_e32 v33, v35
	v_cvt_pk_fp8_f32 v33, v14, v16
	s_add_u32 s14, s16, s14
	s_waitcnt lgkmcnt(1)
	v_med3_f32 v14, v76, s13, v200
	s_waitcnt lgkmcnt(0)
	v_med3_f32 v16, v78, s13, v200
	s_addc_u32 s15, s17, s15
	v_cvt_pk_fp8_f32 v33, v14, v16 op_sel:[0,0,1]
	v_med3_f32 v15, v15, s13, v200
	v_med3_f32 v16, v17, s13, v200
	v_mov_b32_e32 v14, v35
	s_add_u32 s0, s10, s7
	v_med3_f32 v17, v19, s13, v200
	v_cvt_pk_fp8_f32 v14, v15, v16
	v_med3_f32 v16, v53, s13, v200
	v_med3_f32 v19, v71, s13, v200
	v_mov_b32_e32 v15, v35
	s_addc_u32 s1, s11, 0
	v_cvt_pk_fp8_f32 v15, v16, v19
	s_lshl_b64 s[0:1], s[0:1], 10
	v_med3_f32 v18, v18, s13, v200
	v_med3_f32 v20, v20, s13, v200
	s_add_u32 s10, s14, s0
	v_cvt_pk_fp8_f32 v32, v18, v20 op_sel:[0,0,1]
	v_med3_f32 v18, v21, s13, v200
	s_addc_u32 s11, s15, s1
	v_cvt_pk_fp8_f32 v14, v17, v18 op_sel:[0,0,1]
	v_med3_f32 v16, v77, s13, v200
	v_med3_f32 v17, v79, s13, v200
	v_lshl_add_u64 v[80:81], s[10:11], 0, v[4:5]
	s_ashr_i32 s7, s6, 31
	v_cvt_pk_fp8_f32 v15, v16, v17 op_sel:[0,0,1]
	v_lshl_add_u64 v[80:81], v[80:81], 0, s[6:7]
	v_lshl_add_u64 v[16:17], s[10:11], 0, v[6:7]
	v_lshl_add_u64 v[80:81], v[80:81], 0, v[2:3]
	v_lshl_add_u64 v[16:17], v[16:17], 0, s[6:7]
	global_store_dwordx2 v[80:81], v[32:33], off
	v_lshl_add_u64 v[16:17], v[16:17], 0, v[2:3]
	ds_read2_b32 v[18:19], v1 offset0:16 offset1:24
	ds_read2_b32 v[20:21], v1 offset0:49 offset1:57
	ds_read2_b32 v[32:33], v1 offset0:82 offset1:90
	ds_read2_b32 v[52:53], v1 offset0:115 offset1:123
	global_store_dwordx2 v[16:17], v[14:15], off
	ds_read2_b32 v[16:17], v1 offset0:148 offset1:156
	ds_read2_b32 v[70:71], v1 offset0:181 offset1:189
	s_waitcnt lgkmcnt(5)
	v_med3_f32 v15, v18, s13, v200
	s_waitcnt lgkmcnt(4)
	v_med3_f32 v18, v20, s13, v200
	v_mov_b32_e32 v14, v35
	ds_read2_b32 v[76:77], v1 offset0:214 offset1:222
	ds_read2_b32 v[78:79], v1 offset0:247 offset1:255
	v_cvt_pk_fp8_f32 v14, v15, v18
	s_waitcnt lgkmcnt(3)
	v_med3_f32 v16, v16, s13, v200
	s_waitcnt lgkmcnt(2)
	v_med3_f32 v18, v70, s13, v200
	v_mov_b32_e32 v15, v35
	v_cvt_pk_fp8_f32 v15, v16, v18
	v_med3_f32 v20, v32, s13, v200
	v_med3_f32 v22, v52, s13, v200
	s_waitcnt lgkmcnt(1)
	v_med3_f32 v16, v76, s13, v200
	s_waitcnt lgkmcnt(0)
	v_med3_f32 v18, v78, s13, v200
	v_cvt_pk_fp8_f32 v14, v20, v22 op_sel:[0,0,1]
	v_cvt_pk_fp8_f32 v15, v16, v18 op_sel:[0,0,1]
	v_lshl_add_u64 v[80:81], s[10:11], 0, v[8:9]
	v_lshl_add_u64 v[80:81], v[80:81], 0, s[6:7]
	v_lshl_add_u64 v[80:81], v[80:81], 0, v[2:3]
	global_store_dwordx2 v[80:81], v[14:15], off
	v_med3_f32 v15, v19, s13, v200
	v_med3_f32 v16, v21, s13, v200
	v_mov_b32_e32 v14, v35
	v_cvt_pk_fp8_f32 v14, v15, v16
	v_med3_f32 v16, v17, s13, v200
	v_med3_f32 v17, v71, s13, v200
	v_mov_b32_e32 v15, v35
	v_cvt_pk_fp8_f32 v15, v16, v17
	v_med3_f32 v18, v33, s13, v200
	v_med3_f32 v19, v53, s13, v200
	v_med3_f32 v16, v77, s13, v200
	v_med3_f32 v17, v79, s13, v200
	v_cvt_pk_fp8_f32 v14, v18, v19 op_sel:[0,0,1]
	v_cvt_pk_fp8_f32 v15, v16, v17 op_sel:[0,0,1]
	v_lshl_add_u64 v[16:17], s[10:11], 0, v[10:11]
	v_lshl_add_u64 v[16:17], v[16:17], 0, s[6:7]
	v_lshl_add_u64 v[16:17], v[16:17], 0, v[2:3]
	global_store_dwordx2 v[16:17], v[14:15], off
	s_waitcnt lgkmcnt(0)
	s_andn2_b64 vcc, exec, s[8:9]
	s_mov_b64 s[0:1], -1
	s_cbranch_vccnz .LBB0_170
	s_add_i32 s31, s31, s34
	s_add_i32 s35, s35, s36
	s_mov_b64 s[0:1], 0
	s_branch .LBB0_170

.LBB0_776:
	s_andn2_b64 vcc, exec, s[0:1]
	s_waitcnt vmcnt(4)
	v_mov_b32_e32 v15, v22
	v_mov_b32_e32 v16, v23
	v_mov_b32_e32 v17, v24
	v_mov_b32_e32 v18, v27
	v_mov_b32_e32 v19, v31
	v_mov_b32_e32 v20, v37
	v_mov_b32_e32 v21, v42
	v_mov_b32_e32 v25, v56
	v_mov_b32_e32 v26, v57
	v_mov_b32_e32 v28, v58
	v_mov_b32_e32 v29, v59
	v_mov_b32_e32 v30, v60
	v_mov_b32_e32 v32, v61
	v_mov_b32_e32 v33, v62
	v_mov_b32_e32 v36, v63
	v_mov_b32_e32 v38, v64
	v_mov_b32_e32 v39, v65
	v_mov_b32_e32 v40, v66
	v_mov_b32_e32 v41, v67
	v_mov_b32_e32 v43, v68
	v_mov_b32_e32 v44, v69
	v_mov_b32_e32 v45, v70
	v_mov_b32_e32 v46, v71
	v_mov_b32_e32 v47, v72
	v_mov_b32_e32 v48, v73
	v_mov_b32_e32 v49, v74
	v_mov_b32_e32 v50, v75
	v_mov_b32_e32 v51, v76
	v_mov_b32_e32 v52, v77
	v_mov_b32_e32 v53, v78
	v_mov_b32_e32 v54, v79
	v_mov_b32_e32 v55, v80
	s_cbranch_vccz .LBB0_789

.Lmy_cvb_go:
	v_mul_f32_e32 v15, 0x42800000, v15
	s_nop 0
	v_mul_f32_e32 v16, 0x42800000, v16
	ds_write2_b32 v14, v15, v16 offset1:66
	s_nop 0
	v_mul_f32_e32 v15, 0x42800000, v17
	s_nop 0
	v_mul_f32_e32 v16, 0x42800000, v18
	ds_write2_b32 v14, v15, v16 offset0:132 offset1:198
	s_nop 0
	v_mul_f32_e32 v15, 0x42800000, v19
	s_nop 0
	v_mul_f32_e32 v16, 0x42800000, v20
	v_add_u32_e32 v17, 0x400, v14
	ds_write2_b32 v17, v15, v16 offset0:8 offset1:74
	s_nop 0
	v_mul_f32_e32 v15, 0x42800000, v21
	s_nop 0
	v_mul_f32_e32 v16, 0x42800000, v25
	ds_write2_b32 v17, v15, v16 offset0:140 offset1:206
	s_nop 0
	v_mul_f32_e32 v15, 0x42800000, v26
	s_nop 0
	v_mul_f32_e32 v16, 0x42800000, v28
	v_add_u32_e32 v17, 0x800, v14
	ds_write2_b32 v17, v15, v16 offset0:16 offset1:82
	s_nop 0
	v_mul_f32_e32 v15, 0x42800000, v29
	s_nop 0
	v_mul_f32_e32 v16, 0x42800000, v30
	ds_write2_b32 v17, v15, v16 offset0:148 offset1:214
	s_nop 0
	v_mul_f32_e32 v15, 0x42800000, v32
	s_nop 0
	v_mul_f32_e32 v16, 0x42800000, v33
	v_add_u32_e32 v17, 0xc00, v14
	ds_write2_b32 v17, v15, v16 offset0:24 offset1:90
	s_nop 0
	v_mul_f32_e32 v15, 0x42800000, v36
	s_nop 0
	v_mul_f32_e32 v16, 0x42800000, v38
	ds_write2_b32 v17, v15, v16 offset0:156 offset1:222
	s_nop 0
	v_mul_f32_e32 v15, 0x42800000, v39
	s_nop 0
	v_mul_f32_e32 v16, 0x42800000, v40
	v_add_u32_e32 v17, 0x1000, v14
	ds_write2_b32 v17, v15, v16 offset0:32 offset1:98
	s_nop 0
	v_mul_f32_e32 v15, 0x42800000, v41
	s_nop 0
	v_mul_f32_e32 v16, 0x42800000, v43
	ds_write2_b32 v17, v15, v16 offset0:164 offset1:230
	s_nop 0
	v_mul_f32_e32 v15, 0x42800000, v44
	s_nop 0
	v_mul_f32_e32 v16, 0x42800000, v45
	v_add_u32_e32 v17, 0x1400, v14
	ds_write2_b32 v17, v15, v16 offset0:40 offset1:106
	s_nop 0
	v_mul_f32_e32 v15, 0x42800000, v46
	s_nop 0
	v_mul_f32_e32 v16, 0x42800000, v47
	ds_write2_b32 v17, v15, v16 offset0:172 offset1:238
	s_nop 0
	v_mul_f32_e32 v15, 0x42800000, v48
	s_nop 0
	v_mul_f32_e32 v16, 0x42800000, v49
	v_add_u32_e32 v17, 0x1800, v14
	ds_write2_b32 v17, v15, v16 offset0:48 offset1:114
	s_nop 0
	v_mul_f32_e32 v15, 0x42800000, v50
	s_nop 0
	v_mul_f32_e32 v16, 0x42800000, v51
	ds_write2_b32 v17, v15, v16 offset0:180 offset1:246
	s_nop 0
	v_mul_f32_e32 v15, 0x42800000, v52
	s_nop 0
	v_mul_f32_e32 v16, 0x42800000, v53
	v_add_u32_e32 v17, 0x1c00, v14
	ds_write2_b32 v17, v15, v16 offset0:56 offset1:122
	s_nop 0
	v_mul_f32_e32 v15, 0x42800000, v54
	s_nop 0
	v_mul_f32_e32 v16, 0x42800000, v55
	ds_write2_b32 v17, v15, v16 offset0:188 offset1:254
	s_waitcnt lgkmcnt(0)
	ds_read2_b32 v[16:17], v13 offset1:8
	ds_read2_b32 v[18:19], v13 offset0:33 offset1:41
	ds_read2_b32 v[20:21], v13 offset0:66 offset1:74
	ds_read2_b32 v[28:29], v13 offset0:99 offset1:107
	ds_read2_b32 v[38:39], v13 offset0:132 offset1:140
	ds_read2_b32 v[40:41], v13 offset0:165 offset1:173
	s_waitcnt lgkmcnt(5)
	v_med3_f32 v15, v16, s13, v200
	s_waitcnt lgkmcnt(4)
	v_med3_f32 v16, v18, s13, v200
	v_mov_b32_e32 v32, v35
	ds_read2_b32 v[44:45], v13 offset0:198 offset1:206
	ds_read2_b32 v[46:47], v13 offset0:231 offset1:239
	v_cvt_pk_fp8_f32 v32, v15, v16
	s_waitcnt lgkmcnt(3)
	v_med3_f32 v15, v38, s13, v200
	s_waitcnt lgkmcnt(2)
	v_med3_f32 v16, v40, s13, v200
	v_mov_b32_e32 v33, v35
	v_cvt_pk_fp8_f32 v33, v15, v16
	s_add_u32 s22, s16, s22
	s_waitcnt lgkmcnt(1)
	v_med3_f32 v15, v44, s13, v200
	s_waitcnt lgkmcnt(0)
	v_med3_f32 v16, v46, s13, v200
	s_addc_u32 s23, s17, s23
	v_med3_f32 v18, v20, s13, v200
	v_med3_f32 v20, v28, s13, v200
	v_cvt_pk_fp8_f32 v33, v15, v16 op_sel:[0,0,1]
	v_med3_f32 v15, v17, s13, v200
	v_med3_f32 v17, v19, s13, v200
	v_mov_b32_e32 v16, v35
	s_add_u32 s0, s18, s11
	v_cvt_pk_fp8_f32 v32, v18, v20 op_sel:[0,0,1]
	v_cvt_pk_fp8_f32 v16, v15, v17
	v_med3_f32 v15, v39, s13, v200
	v_med3_f32 v20, v41, s13, v200
	v_mov_b32_e32 v17, v35
	s_addc_u32 s1, s19, 0
	v_cvt_pk_fp8_f32 v17, v15, v20
	s_lshl_b64 s[0:1], s[0:1], 10
	s_add_u32 s18, s22, s0
	v_med3_f32 v18, v21, s13, v200
	v_med3_f32 v19, v29, s13, v200
	s_addc_u32 s19, s23, s1
	v_cvt_pk_fp8_f32 v16, v18, v19 op_sel:[0,0,1]
	v_med3_f32 v15, v45, s13, v200
	v_med3_f32 v18, v47, s13, v200
	v_lshl_add_u64 v[48:49], s[18:19], 0, v[4:5]
	s_ashr_i32 s11, s10, 31
	v_cvt_pk_fp8_f32 v17, v15, v18 op_sel:[0,0,1]
	v_lshl_add_u64 v[48:49], v[48:49], 0, s[10:11]
	v_lshl_add_u64 v[18:19], s[18:19], 0, v[6:7]
	v_lshl_add_u64 v[48:49], v[48:49], 0, v[2:3]
	v_lshl_add_u64 v[18:19], v[18:19], 0, s[10:11]
	global_store_dwordx2 v[48:49], v[32:33], off
	v_lshl_add_u64 v[18:19], v[18:19], 0, v[2:3]
	ds_read2_b32 v[20:21], v13 offset0:16 offset1:24
	ds_read2_b32 v[28:29], v13 offset0:49 offset1:57
	ds_read2_b32 v[32:33], v13 offset0:82 offset1:90
	ds_read2_b32 v[38:39], v13 offset0:115 offset1:123
	global_store_dwordx2 v[18:19], v[16:17], off
	ds_read2_b32 v[18:19], v13 offset0:148 offset1:156
	ds_read2_b32 v[40:41], v13 offset0:181 offset1:189
	s_waitcnt lgkmcnt(5)
	v_med3_f32 v15, v20, s13, v200
	s_waitcnt lgkmcnt(4)
	v_med3_f32 v17, v28, s13, v200
	v_mov_b32_e32 v16, v35
	ds_read2_b32 v[44:45], v13 offset0:214 offset1:222
	ds_read2_b32 v[46:47], v13 offset0:247 offset1:255
	v_cvt_pk_fp8_f32 v16, v15, v17
	s_waitcnt lgkmcnt(3)
	v_med3_f32 v15, v18, s13, v200
	s_waitcnt lgkmcnt(2)
	v_med3_f32 v18, v40, s13, v200
	v_mov_b32_e32 v17, v35
	v_cvt_pk_fp8_f32 v17, v15, v18
	v_med3_f32 v20, v32, s13, v200
	v_med3_f32 v25, v38, s13, v200
	s_waitcnt lgkmcnt(1)
	v_med3_f32 v15, v44, s13, v200
	s_waitcnt lgkmcnt(0)
	v_med3_f32 v18, v46, s13, v200
	v_cvt_pk_fp8_f32 v16, v20, v25 op_sel:[0,0,1]
	v_cvt_pk_fp8_f32 v17, v15, v18 op_sel:[0,0,1]
	v_lshl_add_u64 v[48:49], s[18:19], 0, v[8:9]
	v_lshl_add_u64 v[48:49], v[48:49], 0, s[10:11]
	v_lshl_add_u64 v[48:49], v[48:49], 0, v[2:3]
	global_store_dwordx2 v[48:49], v[16:17], off
	v_med3_f32 v15, v21, s13, v200
	v_med3_f32 v17, v29, s13, v200
	v_mov_b32_e32 v16, v35
	v_cvt_pk_fp8_f32 v16, v15, v17
	v_med3_f32 v15, v19, s13, v200
	v_med3_f32 v19, v41, s13, v200
	v_mov_b32_e32 v17, v35
	v_cvt_pk_fp8_f32 v17, v15, v19
	v_med3_f32 v18, v33, s13, v200
	v_med3_f32 v20, v39, s13, v200
	v_cvt_pk_fp8_f32 v16, v18, v20 op_sel:[0,0,1]
	v_med3_f32 v15, v45, s13, v200
	v_med3_f32 v18, v47, s13, v200
	v_cvt_pk_fp8_f32 v17, v15, v18 op_sel:[0,0,1]
	v_lshl_add_u64 v[18:19], s[18:19], 0, v[10:11]
	v_lshl_add_u64 v[18:19], v[18:19], 0, s[10:11]
	v_lshl_add_u64 v[18:19], v[18:19], 0, v[2:3]
	global_store_dwordx2 v[18:19], v[16:17], off
	s_waitcnt lgkmcnt(0)
	s_andn2_b64 vcc, exec, s[14:15]
	s_mov_b64 s[0:1], -1
	s_cbranch_vccnz .LBB0_776
	s_add_i32 s40, s40, s41
	s_add_i32 s42, s42, s43
	s_mov_b64 s[0:1], 0
	s_branch .LBB0_776

.LBB0_1346:
	s_andn2_b64 vcc, exec, s[0:1]
	s_waitcnt vmcnt(4)
	v_mov_b32_e32 v14, v21
	v_mov_b32_e32 v15, v22
	v_mov_b32_e32 v16, v25
	v_mov_b32_e32 v17, v29
	v_mov_b32_e32 v18, v33
	v_mov_b32_e32 v19, v40
	v_mov_b32_e32 v20, v43
	v_mov_b32_e32 v23, v55
	v_mov_b32_e32 v24, v56
	v_mov_b32_e32 v26, v57
	v_mov_b32_e32 v27, v58
	v_mov_b32_e32 v28, v59
	v_mov_b32_e32 v30, v60
	v_mov_b32_e32 v31, v61
	v_mov_b32_e32 v32, v62
	v_mov_b32_e32 v36, v63
	v_mov_b32_e32 v37, v64
	v_mov_b32_e32 v38, v65
	v_mov_b32_e32 v39, v66
	v_mov_b32_e32 v41, v67
	v_mov_b32_e32 v42, v68
	v_mov_b32_e32 v44, v69
	v_mov_b32_e32 v45, v70
	v_mov_b32_e32 v46, v71
	v_mov_b32_e32 v47, v72
	v_mov_b32_e32 v48, v73
	v_mov_b32_e32 v49, v74
	v_mov_b32_e32 v50, v75
	v_mov_b32_e32 v51, v76
	v_mov_b32_e32 v52, v77
	v_mov_b32_e32 v53, v78
	v_mov_b32_e32 v54, v79
	s_cbranch_vccz .LBB0_1359

.Lmy_cvg_go:
	v_mul_f32_e32 v14, 0x42800000, v14
	v_mul_f32_e32 v15, 0x42800000, v15
	ds_write2_b32 v13, v14, v15 offset1:66
	v_mul_f32_e32 v14, 0x42800000, v16
	v_mul_f32_e32 v15, 0x42800000, v17
	ds_write2_b32 v13, v14, v15 offset0:132 offset1:198
	v_mul_f32_e32 v14, 0x42800000, v18
	v_mul_f32_e32 v15, 0x42800000, v19
	v_add_u32_e32 v16, 0x400, v13
	ds_write2_b32 v16, v14, v15 offset0:8 offset1:74
	v_mul_f32_e32 v14, 0x42800000, v20
	v_mul_f32_e32 v15, 0x42800000, v23
	ds_write2_b32 v16, v14, v15 offset0:140 offset1:206
	v_mul_f32_e32 v14, 0x42800000, v24
	v_mul_f32_e32 v15, 0x42800000, v26
	v_add_u32_e32 v16, 0x800, v13
	ds_write2_b32 v16, v14, v15 offset0:16 offset1:82
	v_mul_f32_e32 v14, 0x42800000, v27
	v_mul_f32_e32 v15, 0x42800000, v28
	ds_write2_b32 v16, v14, v15 offset0:148 offset1:214
	v_mul_f32_e32 v14, 0x42800000, v30
	v_mul_f32_e32 v15, 0x42800000, v31
	v_add_u32_e32 v16, 0xc00, v13
	ds_write2_b32 v16, v14, v15 offset0:24 offset1:90
	v_mul_f32_e32 v14, 0x42800000, v32
	v_mul_f32_e32 v15, 0x42800000, v36
	ds_write2_b32 v16, v14, v15 offset0:156 offset1:222
	v_mul_f32_e32 v14, 0x42800000, v37
	v_mul_f32_e32 v15, 0x42800000, v38
	v_add_u32_e32 v16, 0x1000, v13
	ds_write2_b32 v16, v14, v15 offset0:32 offset1:98
	v_mul_f32_e32 v14, 0x42800000, v39
	v_mul_f32_e32 v15, 0x42800000, v41
	ds_write2_b32 v16, v14, v15 offset0:164 offset1:230
	v_mul_f32_e32 v14, 0x42800000, v42
	v_mul_f32_e32 v15, 0x42800000, v44
	v_add_u32_e32 v16, 0x1400, v13
	ds_write2_b32 v16, v14, v15 offset0:40 offset1:106
	v_mul_f32_e32 v14, 0x42800000, v45
	v_mul_f32_e32 v15, 0x42800000, v46
	ds_write2_b32 v16, v14, v15 offset0:172 offset1:238
	v_mul_f32_e32 v14, 0x42800000, v47
	v_mul_f32_e32 v15, 0x42800000, v48
	v_add_u32_e32 v16, 0x1800, v13
	ds_write2_b32 v16, v14, v15 offset0:48 offset1:114
	v_mul_f32_e32 v14, 0x42800000, v49
	v_mul_f32_e32 v15, 0x42800000, v50
	ds_write2_b32 v16, v14, v15 offset0:180 offset1:246
	v_mul_f32_e32 v14, 0x42800000, v51
	v_mul_f32_e32 v15, 0x42800000, v52
	v_add_u32_e32 v16, 0x1c00, v13
	ds_write2_b32 v16, v14, v15 offset0:56 offset1:122
	v_mul_f32_e32 v14, 0x42800000, v53
	v_mul_f32_e32 v15, 0x42800000, v54
	ds_write2_b32 v16, v14, v15 offset0:188 offset1:254
	s_waitcnt lgkmcnt(0)
	ds_read2_b32 v[14:15], v1 offset1:8
	ds_read2_b32 v[16:17], v1 offset0:33 offset1:41
	ds_read2_b32 v[18:19], v1 offset0:66 offset1:74
	ds_read2_b32 v[26:27], v1 offset0:99 offset1:107
	ds_read2_b32 v[36:37], v1 offset0:132 offset1:140
	ds_read2_b32 v[38:39], v1 offset0:165 offset1:173
	s_waitcnt lgkmcnt(0)
	v_med3_f32 v14, v14, s13, v200
	v_med3_f32 v16, v16, s13, v200
	v_mov_b32_e32 v30, v35
	ds_read2_b32 v[44:45], v1 offset0:198 offset1:206
	ds_read2_b32 v[46:47], v1 offset0:231 offset1:239
	v_cvt_pk_fp8_f32 v30, v14, v16
	v_med3_f32 v14, v36, s13, v200
	v_med3_f32 v16, v38, s13, v200
	v_mov_b32_e32 v31, v35
	v_cvt_pk_fp8_f32 v31, v14, v16
	s_add_u32 s14, s16, s14
	s_waitcnt lgkmcnt(1)
	v_med3_f32 v14, v44, s13, v200
	s_waitcnt lgkmcnt(0)
	v_med3_f32 v16, v46, s13, v200
	s_addc_u32 s15, s17, s15
	v_cvt_pk_fp8_f32 v31, v14, v16 op_sel:[0,0,1]
	v_med3_f32 v15, v15, s13, v200
	v_med3_f32 v16, v17, s13, v200
	v_mov_b32_e32 v14, v35
	s_add_u32 s0, s10, s7
	v_med3_f32 v17, v19, s13, v200
	v_cvt_pk_fp8_f32 v14, v15, v16
	v_med3_f32 v16, v37, s13, v200
	v_med3_f32 v19, v39, s13, v200
	v_mov_b32_e32 v15, v35
	s_addc_u32 s1, s11, 0
	v_cvt_pk_fp8_f32 v15, v16, v19
	s_lshl_b64 s[0:1], s[0:1], 10
	v_med3_f32 v18, v18, s13, v200
	v_med3_f32 v20, v26, s13, v200
	s_add_u32 s10, s14, s0
	v_cvt_pk_fp8_f32 v30, v18, v20 op_sel:[0,0,1]
	v_med3_f32 v18, v27, s13, v200
	s_addc_u32 s11, s15, s1
	v_cvt_pk_fp8_f32 v14, v17, v18 op_sel:[0,0,1]
	v_med3_f32 v16, v45, s13, v200
	v_med3_f32 v17, v47, s13, v200
	v_lshl_add_u64 v[48:49], s[10:11], 0, v[4:5]
	s_ashr_i32 s7, s6, 31
	v_cvt_pk_fp8_f32 v15, v16, v17 op_sel:[0,0,1]
	v_lshl_add_u64 v[48:49], v[48:49], 0, s[6:7]
	v_lshl_add_u64 v[16:17], s[10:11], 0, v[6:7]
	v_lshl_add_u64 v[48:49], v[48:49], 0, v[2:3]
	v_lshl_add_u64 v[16:17], v[16:17], 0, s[6:7]
	global_store_dwordx2 v[48:49], v[30:31], off
	v_lshl_add_u64 v[16:17], v[16:17], 0, v[2:3]
	ds_read2_b32 v[18:19], v1 offset0:16 offset1:24
	ds_read2_b32 v[26:27], v1 offset0:49 offset1:57
	ds_read2_b32 v[30:31], v1 offset0:82 offset1:90
	ds_read2_b32 v[36:37], v1 offset0:115 offset1:123
	global_store_dwordx2 v[16:17], v[14:15], off
	ds_read2_b32 v[16:17], v1 offset0:148 offset1:156
	ds_read2_b32 v[38:39], v1 offset0:181 offset1:189
	s_waitcnt lgkmcnt(5)
	v_med3_f32 v15, v18, s13, v200
	s_waitcnt lgkmcnt(4)
	v_med3_f32 v18, v26, s13, v200
	v_mov_b32_e32 v14, v35
	ds_read2_b32 v[44:45], v1 offset0:214 offset1:222
	ds_read2_b32 v[46:47], v1 offset0:247 offset1:255
	v_cvt_pk_fp8_f32 v14, v15, v18
	s_waitcnt lgkmcnt(3)
	v_med3_f32 v16, v16, s13, v200
	s_waitcnt lgkmcnt(2)
	v_med3_f32 v18, v38, s13, v200
	v_mov_b32_e32 v15, v35
	v_cvt_pk_fp8_f32 v15, v16, v18
	v_med3_f32 v20, v30, s13, v200
	v_med3_f32 v23, v36, s13, v200
	s_waitcnt lgkmcnt(1)
	v_med3_f32 v16, v44, s13, v200
	s_waitcnt lgkmcnt(0)
	v_med3_f32 v18, v46, s13, v200
	v_cvt_pk_fp8_f32 v14, v20, v23 op_sel:[0,0,1]
	v_cvt_pk_fp8_f32 v15, v16, v18 op_sel:[0,0,1]
	v_lshl_add_u64 v[48:49], s[10:11], 0, v[8:9]
	v_lshl_add_u64 v[48:49], v[48:49], 0, s[6:7]
	v_lshl_add_u64 v[48:49], v[48:49], 0, v[2:3]
	global_store_dwordx2 v[48:49], v[14:15], off
	v_med3_f32 v15, v19, s13, v200
	v_med3_f32 v16, v27, s13, v200
	v_mov_b32_e32 v14, v35
	v_cvt_pk_fp8_f32 v14, v15, v16
	v_med3_f32 v16, v17, s13, v200
	v_med3_f32 v17, v39, s13, v200
	v_mov_b32_e32 v15, v35
	v_cvt_pk_fp8_f32 v15, v16, v17
	v_med3_f32 v18, v31, s13, v200
	v_med3_f32 v19, v37, s13, v200
	v_med3_f32 v16, v45, s13, v200
	v_med3_f32 v17, v47, s13, v200
	v_cvt_pk_fp8_f32 v14, v18, v19 op_sel:[0,0,1]
	v_cvt_pk_fp8_f32 v15, v16, v17 op_sel:[0,0,1]
	v_lshl_add_u64 v[16:17], s[10:11], 0, v[10:11]
	v_lshl_add_u64 v[16:17], v[16:17], 0, s[6:7]
	v_lshl_add_u64 v[16:17], v[16:17], 0, v[2:3]
	global_store_dwordx2 v[16:17], v[14:15], off
	s_waitcnt lgkmcnt(0)
	s_andn2_b64 vcc, exec, s[8:9]
	s_mov_b64 s[0:1], -1
	s_cbranch_vccnz .LBB0_1346
	s_add_i32 s36, s36, s37
	s_add_i32 s38, s38, s39
	s_mov_b64 s[0:1], 0
	s_branch .LBB0_1346
